# P7 stage B: 32 v_mov per trip removed, pk_fma selects the high half of the ds_read2 pair with op_sel
# speedup vs baseline: 1.0076x; 1.0076x over previous
; template <bool FAST>
; __device__ __forceinline__ void p7_route_t(Frame& F, const bool do_route) {
;     ...
;             for (int it = 0; it < 32; ++it) { const f32x4 w4 = *(const f32x4*)(wp + (size_t)(8 * it) * NE);
; #pragma unroll
;                 for (int r = 0; r < 8; ++r) acc[r] += hp[r * D + 8 * it] * w4; }
.LBB0_825:
	v_mov_b64_e32 v[56:57], v[238:239]
	v_mov_b64_e32 v[58:59], v[240:241]
	v_mov_b64_e32 v[60:61], v[242:243]
	v_mov_b64_e32 v[62:63], v[244:245]
	v_mov_b64_e32 v[64:65], v[246:247]
	v_mov_b64_e32 v[66:67], v[248:249]
	v_mov_b64_e32 v[68:69], v[250:251]
	v_mov_b64_e32 v[70:71], v[252:253]
	s_add_u32 s100, s16, 0x2000
	s_and_b32 s100, s100, 0x7fff
	s_mov_b32 s101, 0
	v_lshl_add_u64 v[176:177], v[42:43], 0, s[100:101]
	v_lshl_add_u64 v[46:47], v[42:43], 0, s[16:17]
	ds_read2_b32 v[44:45], v54 offset1:8
	v_add_u32_e32 v55, 0x2000, v54
	ds_read2_b32 v[48:49], v54 offset0:16 offset1:24
	ds_read2_b32 v[50:51], v54 offset0:32 offset1:40
	ds_read2_b32 v[52:53], v54 offset0:48 offset1:56
	global_load_dwordx4 v[238:241], v[176:177], off
	v_add_u32_e32 v72, 0x4000, v54
	v_add_u32_e32 v73, 0x6000, v54
	v_add_u32_e32 v74, 0x8000, v54
	v_add_u32_e32 v75, 0xa000, v54
	v_add_u32_e32 v110, 0xc000, v54
	v_add_u32_e32 v111, 0xe000, v54
	ds_read2_b32 v[76:77], v55 offset1:8
	ds_read2_b32 v[122:123], v72 offset1:8
	ds_read2_b32 v[124:125], v73 offset1:8
	ds_read2_b32 v[126:127], v74 offset1:8
	ds_read2_b32 v[128:129], v75 offset1:8
	ds_read2_b32 v[130:131], v110 offset1:8
	ds_read2_b32 v[132:133], v111 offset1:8
	global_load_dwordx4 v[242:245], v[176:177], off offset:1024
	ds_read2_b32 v[134:135], v55 offset0:16 offset1:24
	ds_read2_b32 v[136:137], v72 offset0:16 offset1:24
	ds_read2_b32 v[138:139], v73 offset0:16 offset1:24
	ds_read2_b32 v[140:141], v74 offset0:16 offset1:24
	ds_read2_b32 v[142:143], v75 offset0:16 offset1:24
	ds_read2_b32 v[144:145], v110 offset0:16 offset1:24
	ds_read2_b32 v[146:147], v111 offset0:16 offset1:24
	global_load_dwordx4 v[246:249], v[176:177], off offset:2048
	global_load_dwordx4 v[250:253], v[176:177], off offset:3072
	v_add_co_u32_e32 v46, vcc, s92, v46
	ds_read2_b32 v[148:149], v55 offset0:32 offset1:40
	ds_read2_b32 v[150:151], v72 offset0:32 offset1:40
	ds_read2_b32 v[152:153], v73 offset0:32 offset1:40
	ds_read2_b32 v[154:155], v74 offset0:32 offset1:40
	ds_read2_b32 v[156:157], v75 offset0:32 offset1:40
	ds_read2_b32 v[158:159], v110 offset0:32 offset1:40
	ds_read2_b32 v[160:161], v111 offset0:32 offset1:40
	ds_read2_b32 v[162:163], v55 offset0:48 offset1:56
	ds_read2_b32 v[164:165], v72 offset0:48 offset1:56
	ds_read2_b32 v[166:167], v73 offset0:48 offset1:56
	ds_read2_b32 v[168:169], v74 offset0:48 offset1:56
	ds_read2_b32 v[170:171], v75 offset0:48 offset1:56
	ds_read2_b32 v[172:173], v110 offset0:48 offset1:56
	ds_read2_b32 v[174:175], v111 offset0:48 offset1:56
	v_addc_co_u32_e32 v47, vcc, 0, v47, vcc
	global_load_dwordx4 v[72:75], v[46:47], off
	global_load_dwordx4 v[110:113], v[46:47], off offset:1024
	global_load_dwordx4 v[114:117], v[46:47], off offset:2048
	global_load_dwordx4 v[118:121], v[46:47], off offset:3072
	s_waitcnt lgkmcnt(14)
	s_waitcnt lgkmcnt(13)
	s_waitcnt lgkmcnt(12)
	s_waitcnt lgkmcnt(11)
	s_waitcnt lgkmcnt(10)
	s_waitcnt lgkmcnt(9)
	s_waitcnt lgkmcnt(8)
	s_waitcnt lgkmcnt(7)
	s_add_u32 s16, s16, 0x2000
	s_addc_u32 s17, s17, 0
	s_waitcnt lgkmcnt(6)
	s_waitcnt lgkmcnt(5)
	s_waitcnt lgkmcnt(4)
	s_waitcnt lgkmcnt(3)
	s_waitcnt lgkmcnt(2)
	s_waitcnt lgkmcnt(1)
	s_waitcnt lgkmcnt(0)
	v_add_u32_e32 v54, 0x100, v54
	s_cmpk_lg_u32 s16, 0x8000
	v_pk_fma_f32 v[30:31], v[56:57], v[44:45], v[30:31] op_sel_hi:[1,0,1]
	v_pk_fma_f32 v[32:33], v[58:59], v[44:45], v[32:33] op_sel_hi:[1,0,1]
	v_pk_fma_f32 v[26:27], v[56:57], v[76:77], v[26:27] op_sel_hi:[1,0,1]
	v_pk_fma_f32 v[28:29], v[58:59], v[76:77], v[28:29] op_sel_hi:[1,0,1]
	v_pk_fma_f32 v[22:23], v[56:57], v[122:123], v[22:23] op_sel_hi:[1,0,1]
	v_pk_fma_f32 v[24:25], v[58:59], v[122:123], v[24:25] op_sel_hi:[1,0,1]
	v_pk_fma_f32 v[18:19], v[56:57], v[124:125], v[18:19] op_sel_hi:[1,0,1]
	v_pk_fma_f32 v[20:21], v[58:59], v[124:125], v[20:21] op_sel_hi:[1,0,1]
	v_pk_fma_f32 v[14:15], v[56:57], v[126:127], v[14:15] op_sel_hi:[1,0,1]
	v_pk_fma_f32 v[16:17], v[58:59], v[126:127], v[16:17] op_sel_hi:[1,0,1]
	v_pk_fma_f32 v[10:11], v[56:57], v[128:129], v[10:11] op_sel_hi:[1,0,1]
	v_pk_fma_f32 v[12:13], v[58:59], v[128:129], v[12:13] op_sel_hi:[1,0,1]
	v_pk_fma_f32 v[6:7], v[56:57], v[130:131], v[6:7] op_sel_hi:[1,0,1]
	v_pk_fma_f32 v[8:9], v[58:59], v[130:131], v[8:9] op_sel_hi:[1,0,1]
	v_pk_fma_f32 v[2:3], v[56:57], v[132:133], v[2:3] op_sel_hi:[1,0,1]
	v_pk_fma_f32 v[4:5], v[58:59], v[132:133], v[4:5] op_sel_hi:[1,0,1]
	v_pk_fma_f32 v[30:31], v[60:61], v[44:45], v[30:31] op_sel:[0,1,0] op_sel_hi:[1,1,1]
	v_pk_fma_f32 v[32:33], v[62:63], v[44:45], v[32:33] op_sel:[0,1,0] op_sel_hi:[1,1,1]
	v_pk_fma_f32 v[26:27], v[60:61], v[76:77], v[26:27] op_sel:[0,1,0] op_sel_hi:[1,1,1]
	v_pk_fma_f32 v[28:29], v[62:63], v[76:77], v[28:29] op_sel:[0,1,0] op_sel_hi:[1,1,1]
	v_pk_fma_f32 v[22:23], v[60:61], v[122:123], v[22:23] op_sel:[0,1,0] op_sel_hi:[1,1,1]
	v_pk_fma_f32 v[24:25], v[62:63], v[122:123], v[24:25] op_sel:[0,1,0] op_sel_hi:[1,1,1]
	v_pk_fma_f32 v[18:19], v[60:61], v[124:125], v[18:19] op_sel:[0,1,0] op_sel_hi:[1,1,1]
	v_pk_fma_f32 v[20:21], v[62:63], v[124:125], v[20:21] op_sel:[0,1,0] op_sel_hi:[1,1,1]
	v_pk_fma_f32 v[14:15], v[60:61], v[126:127], v[14:15] op_sel:[0,1,0] op_sel_hi:[1,1,1]
	v_pk_fma_f32 v[16:17], v[62:63], v[126:127], v[16:17] op_sel:[0,1,0] op_sel_hi:[1,1,1]
	v_pk_fma_f32 v[10:11], v[60:61], v[128:129], v[10:11] op_sel:[0,1,0] op_sel_hi:[1,1,1]
	v_pk_fma_f32 v[12:13], v[62:63], v[128:129], v[12:13] op_sel:[0,1,0] op_sel_hi:[1,1,1]
	v_pk_fma_f32 v[6:7], v[60:61], v[130:131], v[6:7] op_sel:[0,1,0] op_sel_hi:[1,1,1]
	v_pk_fma_f32 v[8:9], v[62:63], v[130:131], v[8:9] op_sel:[0,1,0] op_sel_hi:[1,1,1]
; template <bool FAST>
; __device__ __forceinline__ void p7_route_t(Frame& F, const bool do_route) {
;     ...
;             for (int it = 0; it < 32; ++it) { const f32x4 w4 = *(const f32x4*)(wp + (size_t)(8 * it) * NE);
; #pragma unroll
;                 for (int r = 0; r < 8; ++r) acc[r] += hp[r * D + 8 * it] * w4; }
	v_pk_fma_f32 v[2:3], v[60:61], v[132:133], v[2:3] op_sel:[0,1,0] op_sel_hi:[1,1,1]
	v_pk_fma_f32 v[4:5], v[62:63], v[132:133], v[4:5] op_sel:[0,1,0] op_sel_hi:[1,1,1]
	v_pk_fma_f32 v[32:33], v[66:67], v[48:49], v[32:33] op_sel_hi:[1,0,1]
	v_pk_fma_f32 v[30:31], v[64:65], v[48:49], v[30:31] op_sel_hi:[1,0,1]
	v_pk_fma_f32 v[28:29], v[66:67], v[134:135], v[28:29] op_sel_hi:[1,0,1]
	v_pk_fma_f32 v[26:27], v[64:65], v[134:135], v[26:27] op_sel_hi:[1,0,1]
	v_pk_fma_f32 v[24:25], v[66:67], v[136:137], v[24:25] op_sel_hi:[1,0,1]
	v_pk_fma_f32 v[22:23], v[64:65], v[136:137], v[22:23] op_sel_hi:[1,0,1]
	v_pk_fma_f32 v[20:21], v[66:67], v[138:139], v[20:21] op_sel_hi:[1,0,1]
	v_pk_fma_f32 v[18:19], v[64:65], v[138:139], v[18:19] op_sel_hi:[1,0,1]
	v_pk_fma_f32 v[16:17], v[66:67], v[140:141], v[16:17] op_sel_hi:[1,0,1]
	v_pk_fma_f32 v[14:15], v[64:65], v[140:141], v[14:15] op_sel_hi:[1,0,1]
	v_pk_fma_f32 v[12:13], v[66:67], v[142:143], v[12:13] op_sel_hi:[1,0,1]
	v_pk_fma_f32 v[10:11], v[64:65], v[142:143], v[10:11] op_sel_hi:[1,0,1]
	v_pk_fma_f32 v[8:9], v[66:67], v[144:145], v[8:9] op_sel_hi:[1,0,1]
	v_pk_fma_f32 v[6:7], v[64:65], v[144:145], v[6:7] op_sel_hi:[1,0,1]
	v_pk_fma_f32 v[4:5], v[66:67], v[146:147], v[4:5] op_sel_hi:[1,0,1]
	v_pk_fma_f32 v[2:3], v[64:65], v[146:147], v[2:3] op_sel_hi:[1,0,1]
	v_pk_fma_f32 v[30:31], v[68:69], v[48:49], v[30:31] op_sel:[0,1,0] op_sel_hi:[1,1,1]
	v_pk_fma_f32 v[32:33], v[70:71], v[48:49], v[32:33] op_sel:[0,1,0] op_sel_hi:[1,1,1]
	v_pk_fma_f32 v[26:27], v[68:69], v[134:135], v[26:27] op_sel:[0,1,0] op_sel_hi:[1,1,1]
	v_pk_fma_f32 v[28:29], v[70:71], v[134:135], v[28:29] op_sel:[0,1,0] op_sel_hi:[1,1,1]
	v_pk_fma_f32 v[22:23], v[68:69], v[136:137], v[22:23] op_sel:[0,1,0] op_sel_hi:[1,1,1]
	v_pk_fma_f32 v[24:25], v[70:71], v[136:137], v[24:25] op_sel:[0,1,0] op_sel_hi:[1,1,1]
	v_pk_fma_f32 v[18:19], v[68:69], v[138:139], v[18:19] op_sel:[0,1,0] op_sel_hi:[1,1,1]
	v_pk_fma_f32 v[20:21], v[70:71], v[138:139], v[20:21] op_sel:[0,1,0] op_sel_hi:[1,1,1]
	v_pk_fma_f32 v[14:15], v[68:69], v[140:141], v[14:15] op_sel:[0,1,0] op_sel_hi:[1,1,1]
	v_pk_fma_f32 v[16:17], v[70:71], v[140:141], v[16:17] op_sel:[0,1,0] op_sel_hi:[1,1,1]
	v_pk_fma_f32 v[10:11], v[68:69], v[142:143], v[10:11] op_sel:[0,1,0] op_sel_hi:[1,1,1]
	v_pk_fma_f32 v[12:13], v[70:71], v[142:143], v[12:13] op_sel:[0,1,0] op_sel_hi:[1,1,1]
	v_pk_fma_f32 v[6:7], v[68:69], v[144:145], v[6:7] op_sel:[0,1,0] op_sel_hi:[1,1,1]
	v_pk_fma_f32 v[8:9], v[70:71], v[144:145], v[8:9] op_sel:[0,1,0] op_sel_hi:[1,1,1]
	v_pk_fma_f32 v[2:3], v[68:69], v[146:147], v[2:3] op_sel:[0,1,0] op_sel_hi:[1,1,1]
	v_pk_fma_f32 v[4:5], v[70:71], v[146:147], v[4:5] op_sel:[0,1,0] op_sel_hi:[1,1,1]
	s_waitcnt vmcnt(3)
	v_pk_fma_f32 v[32:33], v[74:75], v[50:51], v[32:33] op_sel_hi:[1,0,1]
	v_pk_fma_f32 v[30:31], v[72:73], v[50:51], v[30:31] op_sel_hi:[1,0,1]
	v_pk_fma_f32 v[28:29], v[74:75], v[148:149], v[28:29] op_sel_hi:[1,0,1]
	v_pk_fma_f32 v[26:27], v[72:73], v[148:149], v[26:27] op_sel_hi:[1,0,1]
	v_pk_fma_f32 v[24:25], v[74:75], v[150:151], v[24:25] op_sel_hi:[1,0,1]
	v_pk_fma_f32 v[22:23], v[72:73], v[150:151], v[22:23] op_sel_hi:[1,0,1]
	v_pk_fma_f32 v[20:21], v[74:75], v[152:153], v[20:21] op_sel_hi:[1,0,1]
	v_pk_fma_f32 v[18:19], v[72:73], v[152:153], v[18:19] op_sel_hi:[1,0,1]
	v_pk_fma_f32 v[16:17], v[74:75], v[154:155], v[16:17] op_sel_hi:[1,0,1]
	v_pk_fma_f32 v[14:15], v[72:73], v[154:155], v[14:15] op_sel_hi:[1,0,1]
	v_pk_fma_f32 v[12:13], v[74:75], v[156:157], v[12:13] op_sel_hi:[1,0,1]
	v_pk_fma_f32 v[10:11], v[72:73], v[156:157], v[10:11] op_sel_hi:[1,0,1]
	v_pk_fma_f32 v[8:9], v[74:75], v[158:159], v[8:9] op_sel_hi:[1,0,1]
	v_pk_fma_f32 v[6:7], v[72:73], v[158:159], v[6:7] op_sel_hi:[1,0,1]
	v_pk_fma_f32 v[4:5], v[74:75], v[160:161], v[4:5] op_sel_hi:[1,0,1]
	v_pk_fma_f32 v[2:3], v[72:73], v[160:161], v[2:3] op_sel_hi:[1,0,1]
	s_waitcnt vmcnt(2)
	v_pk_fma_f32 v[32:33], v[112:113], v[50:51], v[32:33] op_sel:[0,1,0] op_sel_hi:[1,1,1]
	v_pk_fma_f32 v[30:31], v[110:111], v[50:51], v[30:31] op_sel:[0,1,0] op_sel_hi:[1,1,1]
	v_pk_fma_f32 v[28:29], v[112:113], v[148:149], v[28:29] op_sel:[0,1,0] op_sel_hi:[1,1,1]
	v_pk_fma_f32 v[26:27], v[110:111], v[148:149], v[26:27] op_sel:[0,1,0] op_sel_hi:[1,1,1]
	v_pk_fma_f32 v[24:25], v[112:113], v[150:151], v[24:25] op_sel:[0,1,0] op_sel_hi:[1,1,1]
	v_pk_fma_f32 v[22:23], v[110:111], v[150:151], v[22:23] op_sel:[0,1,0] op_sel_hi:[1,1,1]
	v_pk_fma_f32 v[20:21], v[112:113], v[152:153], v[20:21] op_sel:[0,1,0] op_sel_hi:[1,1,1]
	v_pk_fma_f32 v[18:19], v[110:111], v[152:153], v[18:19] op_sel:[0,1,0] op_sel_hi:[1,1,1]
	v_pk_fma_f32 v[16:17], v[112:113], v[154:155], v[16:17] op_sel:[0,1,0] op_sel_hi:[1,1,1]
	v_pk_fma_f32 v[14:15], v[110:111], v[154:155], v[14:15] op_sel:[0,1,0] op_sel_hi:[1,1,1]
	v_pk_fma_f32 v[12:13], v[112:113], v[156:157], v[12:13] op_sel:[0,1,0] op_sel_hi:[1,1,1]
	v_pk_fma_f32 v[10:11], v[110:111], v[156:157], v[10:11] op_sel:[0,1,0] op_sel_hi:[1,1,1]
	v_pk_fma_f32 v[8:9], v[112:113], v[158:159], v[8:9] op_sel:[0,1,0] op_sel_hi:[1,1,1]
	v_pk_fma_f32 v[6:7], v[110:111], v[158:159], v[6:7] op_sel:[0,1,0] op_sel_hi:[1,1,1]
	v_pk_fma_f32 v[4:5], v[112:113], v[160:161], v[4:5] op_sel:[0,1,0] op_sel_hi:[1,1,1]
	v_pk_fma_f32 v[2:3], v[110:111], v[160:161], v[2:3] op_sel:[0,1,0] op_sel_hi:[1,1,1]
	s_waitcnt vmcnt(1)
; #define LAS __attribute__((address_space(3)))
; template <int CTRL> __device__ __forceinline__ float dpp_add(float x) { return x + __builtin_bit_cast(float, __builtin_amdgcn_update_dpp(0, __builtin_bit_cast(int, x), CTRL, 0xF, 0xF, true)); }
; template <bool FAST>
; __device__ __forceinline__ void p7_route_t(Frame& F, const bool do_route) {
;     ...
;             for (int it = 0; it < 32; ++it) { const f32x4 w4 = *(const f32x4*)(wp + (size_t)(8 * it) * NE);
; #pragma unroll
;                 for (int r = 0; r < 8; ++r) acc[r] += hp[r * D + 8 * it] * w4; }
; #pragma unroll
;             for (int r = 0; r < 8; ++r) { acc[r].x = dpp_add<0x128>(acc[r].x); acc[r].y = dpp_add<0x128>(acc[r].y); acc[r].z = dpp_add<0x128>(acc[r].z); acc[r].w = dpp_add<0x128>(acc[r].w); }
;             if (!(cg & 1)) {
; #pragma unroll
;                 for (int r = 0; r < 8; ++r) *(LAS f32x4*)(part + ((F.wave * 4 + (cg >> 1)) * 8 + r) * 32 + 4 * eq) = acc[r]; }
	v_pk_fma_f32 v[32:33], v[116:117], v[52:53], v[32:33] op_sel_hi:[1,0,1]
	v_pk_fma_f32 v[30:31], v[114:115], v[52:53], v[30:31] op_sel_hi:[1,0,1]
	v_pk_fma_f32 v[28:29], v[116:117], v[162:163], v[28:29] op_sel_hi:[1,0,1]
	v_pk_fma_f32 v[26:27], v[114:115], v[162:163], v[26:27] op_sel_hi:[1,0,1]
	v_pk_fma_f32 v[24:25], v[116:117], v[164:165], v[24:25] op_sel_hi:[1,0,1]
	v_pk_fma_f32 v[22:23], v[114:115], v[164:165], v[22:23] op_sel_hi:[1,0,1]
	v_pk_fma_f32 v[20:21], v[116:117], v[166:167], v[20:21] op_sel_hi:[1,0,1]
	v_pk_fma_f32 v[18:19], v[114:115], v[166:167], v[18:19] op_sel_hi:[1,0,1]
	v_pk_fma_f32 v[16:17], v[116:117], v[168:169], v[16:17] op_sel_hi:[1,0,1]
	v_pk_fma_f32 v[14:15], v[114:115], v[168:169], v[14:15] op_sel_hi:[1,0,1]
	v_pk_fma_f32 v[12:13], v[116:117], v[170:171], v[12:13] op_sel_hi:[1,0,1]
	v_pk_fma_f32 v[10:11], v[114:115], v[170:171], v[10:11] op_sel_hi:[1,0,1]
	v_pk_fma_f32 v[8:9], v[116:117], v[172:173], v[8:9] op_sel_hi:[1,0,1]
	v_pk_fma_f32 v[6:7], v[114:115], v[172:173], v[6:7] op_sel_hi:[1,0,1]
	v_pk_fma_f32 v[4:5], v[116:117], v[174:175], v[4:5] op_sel_hi:[1,0,1]
	v_pk_fma_f32 v[2:3], v[114:115], v[174:175], v[2:3] op_sel_hi:[1,0,1]
	s_waitcnt vmcnt(0)
	v_pk_fma_f32 v[32:33], v[120:121], v[52:53], v[32:33] op_sel:[0,1,0] op_sel_hi:[1,1,1]
	v_pk_fma_f32 v[30:31], v[118:119], v[52:53], v[30:31] op_sel:[0,1,0] op_sel_hi:[1,1,1]
	v_pk_fma_f32 v[28:29], v[120:121], v[162:163], v[28:29] op_sel:[0,1,0] op_sel_hi:[1,1,1]
	v_pk_fma_f32 v[26:27], v[118:119], v[162:163], v[26:27] op_sel:[0,1,0] op_sel_hi:[1,1,1]
	v_pk_fma_f32 v[24:25], v[120:121], v[164:165], v[24:25] op_sel:[0,1,0] op_sel_hi:[1,1,1]
	v_pk_fma_f32 v[22:23], v[118:119], v[164:165], v[22:23] op_sel:[0,1,0] op_sel_hi:[1,1,1]
	v_pk_fma_f32 v[20:21], v[120:121], v[166:167], v[20:21] op_sel:[0,1,0] op_sel_hi:[1,1,1]
	v_pk_fma_f32 v[18:19], v[118:119], v[166:167], v[18:19] op_sel:[0,1,0] op_sel_hi:[1,1,1]
	v_pk_fma_f32 v[16:17], v[120:121], v[168:169], v[16:17] op_sel:[0,1,0] op_sel_hi:[1,1,1]
	v_pk_fma_f32 v[14:15], v[118:119], v[168:169], v[14:15] op_sel:[0,1,0] op_sel_hi:[1,1,1]
	v_pk_fma_f32 v[12:13], v[120:121], v[170:171], v[12:13] op_sel:[0,1,0] op_sel_hi:[1,1,1]
	v_pk_fma_f32 v[10:11], v[118:119], v[170:171], v[10:11] op_sel:[0,1,0] op_sel_hi:[1,1,1]
	v_pk_fma_f32 v[8:9], v[120:121], v[172:173], v[8:9] op_sel:[0,1,0] op_sel_hi:[1,1,1]
	v_pk_fma_f32 v[6:7], v[118:119], v[172:173], v[6:7] op_sel:[0,1,0] op_sel_hi:[1,1,1]
	v_pk_fma_f32 v[4:5], v[120:121], v[174:175], v[4:5] op_sel:[0,1,0] op_sel_hi:[1,1,1]
	v_pk_fma_f32 v[2:3], v[118:119], v[174:175], v[2:3] op_sel:[0,1,0] op_sel_hi:[1,1,1]
	s_cbranch_scc1 .LBB0_825
	v_mov_b32_dpp v72, v30 row_ror:8 row_mask:0xf bank_mask:0xf bound_ctrl:1
	v_mov_b32_dpp v73, v31 row_ror:8 row_mask:0xf bank_mask:0xf bound_ctrl:1
	v_mov_b32_dpp v74, v32 row_ror:8 row_mask:0xf bank_mask:0xf bound_ctrl:1
	v_mov_b32_dpp v75, v33 row_ror:8 row_mask:0xf bank_mask:0xf bound_ctrl:1
	v_mov_b32_dpp v68, v26 row_ror:8 row_mask:0xf bank_mask:0xf bound_ctrl:1
	v_mov_b32_dpp v69, v27 row_ror:8 row_mask:0xf bank_mask:0xf bound_ctrl:1
	v_mov_b32_dpp v70, v28 row_ror:8 row_mask:0xf bank_mask:0xf bound_ctrl:1
	v_mov_b32_dpp v71, v29 row_ror:8 row_mask:0xf bank_mask:0xf bound_ctrl:1
	v_mov_b32_dpp v64, v22 row_ror:8 row_mask:0xf bank_mask:0xf bound_ctrl:1
	v_mov_b32_dpp v65, v23 row_ror:8 row_mask:0xf bank_mask:0xf bound_ctrl:1
	v_mov_b32_dpp v66, v24 row_ror:8 row_mask:0xf bank_mask:0xf bound_ctrl:1
	v_mov_b32_dpp v67, v25 row_ror:8 row_mask:0xf bank_mask:0xf bound_ctrl:1
	v_mov_b32_dpp v60, v18 row_ror:8 row_mask:0xf bank_mask:0xf bound_ctrl:1
	v_mov_b32_dpp v61, v19 row_ror:8 row_mask:0xf bank_mask:0xf bound_ctrl:1
	v_mov_b32_dpp v62, v20 row_ror:8 row_mask:0xf bank_mask:0xf bound_ctrl:1
	v_mov_b32_dpp v63, v21 row_ror:8 row_mask:0xf bank_mask:0xf bound_ctrl:1
	v_mov_b32_dpp v56, v14 row_ror:8 row_mask:0xf bank_mask:0xf bound_ctrl:1
	v_mov_b32_dpp v57, v15 row_ror:8 row_mask:0xf bank_mask:0xf bound_ctrl:1
	v_mov_b32_dpp v58, v16 row_ror:8 row_mask:0xf bank_mask:0xf bound_ctrl:1
	v_mov_b32_dpp v59, v17 row_ror:8 row_mask:0xf bank_mask:0xf bound_ctrl:1
	v_mov_b32_dpp v52, v10 row_ror:8 row_mask:0xf bank_mask:0xf bound_ctrl:1
	v_mov_b32_dpp v53, v11 row_ror:8 row_mask:0xf bank_mask:0xf bound_ctrl:1
	v_mov_b32_dpp v54, v12 row_ror:8 row_mask:0xf bank_mask:0xf bound_ctrl:1
	v_mov_b32_dpp v55, v13 row_ror:8 row_mask:0xf bank_mask:0xf bound_ctrl:1
	v_mov_b32_dpp v48, v6 row_ror:8 row_mask:0xf bank_mask:0xf bound_ctrl:1
	v_mov_b32_dpp v49, v7 row_ror:8 row_mask:0xf bank_mask:0xf bound_ctrl:1
	v_mov_b32_dpp v50, v8 row_ror:8 row_mask:0xf bank_mask:0xf bound_ctrl:1
	v_mov_b32_dpp v51, v9 row_ror:8 row_mask:0xf bank_mask:0xf bound_ctrl:1
	v_mov_b32_dpp v44, v2 row_ror:8 row_mask:0xf bank_mask:0xf bound_ctrl:1
	v_mov_b32_dpp v45, v3 row_ror:8 row_mask:0xf bank_mask:0xf bound_ctrl:1
	v_mov_b32_dpp v46, v4 row_ror:8 row_mask:0xf bank_mask:0xf bound_ctrl:1
	v_mov_b32_dpp v47, v5 row_ror:8 row_mask:0xf bank_mask:0xf bound_ctrl:1
	s_and_saveexec_b64 s[2:3], s[6:7]
	s_cbranch_execz .LBB0_828
	v_pk_add_f32 v[32:33], v[32:33], v[74:75]
	v_pk_add_f32 v[30:31], v[30:31], v[72:73]
	v_pk_add_f32 v[28:29], v[28:29], v[70:71]
	v_pk_add_f32 v[26:27], v[26:27], v[68:69]
	v_pk_add_f32 v[24:25], v[24:25], v[66:67]
	v_pk_add_f32 v[22:23], v[22:23], v[64:65]
	v_pk_add_f32 v[20:21], v[20:21], v[62:63]
	v_pk_add_f32 v[18:19], v[18:19], v[60:61]
	v_pk_add_f32 v[16:17], v[16:17], v[58:59]
	v_pk_add_f32 v[14:15], v[14:15], v[56:57]
	v_pk_add_f32 v[12:13], v[12:13], v[54:55]
	v_pk_add_f32 v[10:11], v[10:11], v[52:53]
	v_pk_add_f32 v[8:9], v[8:9], v[50:51]
	v_pk_add_f32 v[6:7], v[6:7], v[48:49]
	v_pk_add_f32 v[4:5], v[4:5], v[46:47]
	v_pk_add_f32 v[2:3], v[2:3], v[44:45]
	ds_write_b128 v107, v[30:33]
	ds_write_b128 v107, v[26:29] offset:128
	ds_write_b128 v107, v[22:25] offset:256
	ds_write_b128 v107, v[18:21] offset:384
	ds_write_b128 v107, v[14:17] offset:512
	ds_write_b128 v107, v[10:13] offset:640
	ds_write_b128 v107, v[6:9] offset:768
	ds_write_b128 v107, v[2:5] offset:896
